# cache loads issued right behind the slot-table loads (counted waits widened)
# baseline (speedup 1.0000x reference)
_Z6k_iterILb0ELb0EEvPKfS1_PKiPK15HIP_vector_typeIfLj4EES7_S1_S1_S3_S1_PfS8_S1_S3_PDF16_PS5_SA_PiSA_SB_:
	s_and_b32 s38, s0, 0xfffff000
	s_mov_b32 s39, s1
	s_load_dwordx2 s[8:9], s[0:1], 0x80
	s_load_dwordx4 s[4:7], s[0:1], 0x70
	s_load_dwordx4 s[16:19], s[0:1], 0x40
	s_load_dwordx2 s[40:41], s[0:1], 0x90
	s_load_dwordx2 s[42:43], s[0:1], 0x88
	v_readfirstlane_b32 s12, v0
	v_cmp_gt_u32_e64 s[14:15], 64, v0
	v_lshlrev_b32_e32 v1, 2, v0
	s_and_saveexec_b64 s[10:11], s[14:15]
	v_mov_b32_e32 v2, 0
	ds_write_b32 v1, v2 offset:5152
	s_or_b64 exec, exec, s[10:11]
	s_lshl_b32 s3, s2, 5
	s_and_b32 s3, s3, 0xe0
	s_lshr_b32 s2, s2, 3
	s_add_i32 s2, s3, s2
	s_lshl_b32 s25, s2, 6
	v_and_b32_e32 v2, 31, v0
	v_or_b32_e32 v4, s25, v2
	v_mov_b32_e32 v5, 0
	s_lshr_b32 s27, s12, 6
	s_lshl_b32 s32, s27, 2
	s_lshr_b32 s32, 0x73261540, s32
	s_lshl_b32 s32, s32, 5
	s_and_b32 s32, s32, 0xe0
	v_or_b32_e32 v176, s32, v2
	v_lshlrev_b32_e32 v177, 4, v176
	v_add_u32_e32 v178, 0x1000, v177
	v_add_u32_e32 v179, 0x2000, v177
	v_add_u32_e32 v180, 0x3000, v177
	v_add_u32_e32 v181, 0x4000, v177
	v_add_u32_e32 v182, 0x5000, v177
	s_mov_b32 s3, 0
	s_lshl_b64 s[34:35], s[2:3], 16
	s_lshl_b32 s33, s2, 2
	s_waitcnt lgkmcnt(0)
	s_load_dword s24, s[8:9], s33 offset:0x0
	s_load_dword s41, s[40:41], s33 offset:0x0
	s_add_u32 s20, s4, s34
	s_addc_u32 s21, s5, s35
	v_lshl_add_u64 v[4:5], v[4:5], 4, s[6:7]
	global_load_dwordx3 v[30:32], v[4:5], off
	global_load_dwordx3 v[26:28], v[4:5], off offset:512
	global_load_dwordx4 v[2:5], v177, s[20:21]
	global_load_dwordx4 v[6:9], v178, s[20:21]
	global_load_dwordx4 v[10:13], v179, s[20:21]
	global_load_dwordx4 v[14:17], v180, s[20:21]
	global_load_dwordx4 v[18:21], v181, s[20:21]
	global_load_dwordx4 v[22:25], v182, s[20:21]
	s_lshl_b32 s46, s27, 12
	s_add_u32 s46, s46, 0x8000
	s_add_u32 s44, s20, s46
	s_addc_u32 s45, s21, 0
	s_add_u32 s36, s42, s34
	s_addc_u32 s37, s43, s35
	s_add_u32 s36, s36, s46
	s_addc_u32 s37, s37, 0
	v_and_b32_e32 v183, 63, v0
	v_lshlrev_b32_e32 v183, 4, v183
	global_load_dwordx4 v[184:187], v183, s[44:45]
	global_load_dwordx4 v[188:191], v183, s[44:45] offset:1024
	global_load_dwordx4 v[192:195], v183, s[44:45] offset:2048
	global_load_dwordx4 v[196:199], v183, s[44:45] offset:3072
	global_load_dwordx4 v[200:203], v183, s[36:37]
	global_load_dwordx4 v[204:207], v183, s[36:37] offset:1024
	global_load_dwordx4 v[208:211], v183, s[36:37] offset:2048
	global_load_dwordx4 v[212:215], v183, s[36:37] offset:3072
	v_and_b32_e32 v38, 63, v0
	v_mov_b32_e32 v29, 0xff800000
	v_cmp_gt_u32_e64 s[0:1], 32, v38
	s_waitcnt lgkmcnt(0)
	s_cmpk_gt_i32 s24, 0x600
	s_cselect_b64 s[22:23], -1, 0
	s_cmpk_lt_i32 s24, 0x601
	s_cbranch_scc1 .LBB3_6
	s_and_saveexec_b64 s[8:9], s[14:15]
	s_cbranch_execz .LBB3_5
	v_or_b32_e32 v178, s25, v0
	v_mov_b32_e32 v179, 0
	v_lshl_add_u64 v[178:179], v[178:179], 4, s[6:7]
	global_load_dwordx4 v[178:181], v[178:179], off
	v_lshlrev_b32_e32 v177, 4, v0
	s_waitcnt vmcnt(0)
	ds_write_b128 v177, v[178:181] offset:2080

.LBB3_6:
	s_xor_b32 s33, s32, 0xff
	s_add_i32 s33, s33, s24
	s_ashr_i32 s26, s33, 8
	v_cmp_gt_i32_e32 vcc, s24, v176
	v_med3_i32 v33, s26, 0, 6
	s_sub_i32 s33, s24, 0x100
	v_cmp_gt_i32_e64 s[4:5], s33, v176
	s_sub_i32 s33, s24, 0x200
	v_cmp_gt_i32_e64 s[6:7], s33, v176
	s_sub_i32 s33, s24, 0x300
	v_cmp_gt_i32_e64 s[8:9], s33, v176
	s_sub_i32 s33, s24, 0x400
	v_cmp_gt_i32_e64 s[10:11], s33, v176
	s_sub_i32 s33, s24, 0x500
	v_cmp_gt_i32_e64 s[12:13], s33, v176
	s_and_b32 s25, s25, 0x7ffff000
	s_mov_b32 s2, 0xffff0000
	v_readfirstlane_b32 s26, v33
	s_nop 3
	s_cmp_lt_i32 s26, 4
	s_waitcnt vmcnt(13)
	v_cndmask_b32_e32 v4, v29, v4, vcc
	v_cndmask_b32_e64 v134, v3, v2, s[0:1]
	v_cndmask_b32_e32 v134, 0, v134, vcc
	s_waitcnt vmcnt(12)
	v_cndmask_b32_e64 v3, v29, v8, s[4:5]
	v_cndmask_b32_e64 v97, v7, v6, s[0:1]
	v_cndmask_b32_e64 v97, 0, v97, s[4:5]
	v_cndmask_b32_e64 v135, 1.0, v4, s[0:1]
	v_cndmask_b32_e64 v33, -1, v9, s[4:5]
	v_cndmask_b32_e64 v98, 1.0, v3, s[0:1]
	s_waitcnt vmcnt(11)
	v_cndmask_b32_e64 v6, v29, v12, s[6:7]
	v_cndmask_b32_e64 v68, v11, v10, s[0:1]
	v_cndmask_b32_e64 v68, 0, v68, s[6:7]
	s_waitcnt vmcnt(10)
	v_cndmask_b32_e64 v7, v29, v16, s[8:9]
	v_cndmask_b32_e64 v70, 1.0, v6, s[0:1]
	v_cndmask_b32_e64 v73, 1.0, v7, s[0:1]
	v_cndmask_b32_e64 v34, -1, v13, s[6:7]
	v_cndmask_b32_e64 v35, -1, v17, s[8:9]
	v_cndmask_b32_e64 v71, v15, v14, s[0:1]
	v_cndmask_b32_e64 v71, 0, v71, s[8:9]
	s_waitcnt vmcnt(9)
	v_cndmask_b32_e64 v8, v29, v20, s[10:11]
	v_cndmask_b32_e64 v48, 1.0, v8, s[0:1]
	s_waitcnt vmcnt(8)
	v_cndmask_b32_e64 v10, v29, v24, s[12:13]
	v_cndmask_b32_e32 v29, -1, v5, vcc
	v_max_i32_e32 v4, 0, v29
	v_add_u32_e32 v4, s25, v4
	v_mov_b32_e32 v5, 0
	v_lshl_add_u64 v[6:7], v[4:5], 2, s[16:17]
	v_max_i32_e32 v4, 0, v33
	v_add_u32_e32 v4, s25, v4
	v_lshl_add_u64 v[8:9], v[4:5], 2, s[16:17]
	v_max_i32_e32 v4, 0, v34
	v_add_u32_e32 v4, s25, v4
	v_cndmask_b32_e64 v3, 1.0, v10, s[0:1]
	v_lshl_add_u64 v[10:11], v[4:5], 2, s[16:17]
	v_max_i32_e32 v4, 0, v35
	v_cndmask_b32_e64 v36, -1, v21, s[10:11]
	v_add_u32_e32 v4, s25, v4
	v_lshl_add_u64 v[12:13], v[4:5], 2, s[16:17]
	v_max_i32_e32 v4, 0, v36
	v_cndmask_b32_e64 v37, -1, v25, s[12:13]
	v_add_u32_e32 v4, s25, v4
	v_lshl_add_u64 v[14:15], v[4:5], 2, s[16:17]
	v_max_i32_e32 v4, 0, v37
	v_cndmask_b32_e64 v46, v19, v18, s[0:1]
	v_cndmask_b32_e64 v46, 0, v46, s[10:11]
	v_cndmask_b32_e64 v2, v23, v22, s[0:1]
	v_cndmask_b32_e64 v2, 0, v2, s[12:13]
	v_add_u32_e32 v4, s25, v4
	v_lshl_add_u64 v[4:5], v[4:5], 2, s[16:17]
	s_cmpk_lt_i32 s24, 0x801
	s_cselect_b32 s47, 1, 0
	s_cbranch_scc0 .Lffc_nocache
	s_lshl_b32 s46, s27, 12
	s_add_u32 s46, s46, 0x8000
	s_add_u32 s44, s20, s46
	s_addc_u32 s45, s21, 0
	v_lshlrev_b32_e32 v183, 4, v38
.Lffc_nocache:
	s_cmpk_lt_i32 s41, 0x801
	s_cselect_b32 s36, 1, 0
	s_cbranch_scc0 .Lffc_nocache1
	s_lshl_b32 s46, s27, 12
	s_add_u32 s46, s46, 0x8000
	s_add_u32 s44, s42, s34
	s_addc_u32 s45, s43, s35
	s_add_u32 s44, s44, s46
	s_addc_u32 s45, s45, 0
	v_lshlrev_b32_e32 v183, 4, v38
.Lffc_nocache1:
	s_cmp_lt_i32 s26, 4
	global_load_dword v133, v[6:7], off
	global_load_dword v132, v[8:9], off
	global_load_dword v131, v[10:11], off
	global_load_dword v130, v[12:13], off
	global_load_dword v129, v[14:15], off
	global_load_dword v128, v[4:5], off
	v_max_f32_e32 v6, v32, v32
	v_cndmask_b32_e64 v4, v31, v30, s[0:1]
	v_max_f32_e32 v6, 0xc6ea6000, v6
	v_cndmask_b32_e64 v6, v6, 1.0, s[0:1]
	v_and_b32_e32 v7, 0xffff0000, v4
	v_sub_f32_e32 v8, v4, v7
	v_or_b32_sdwa v22, v4, v7 dst_sel:DWORD dst_unused:UNUSED_PAD src0_sel:WORD_1 src1_sel:DWORD
	v_and_b32_e32 v4, 0xffff0000, v6
	v_sub_f32_e32 v7, v6, v4
	v_or_b32_sdwa v24, v6, v4 dst_sel:DWORD dst_unused:UNUSED_PAD src0_sel:WORD_1 src1_sel:DWORD
	v_or_b32_sdwa v23, v8, v4 dst_sel:DWORD dst_unused:UNUSED_PAD src0_sel:WORD_1 src1_sel:DWORD
	v_max_f32_e32 v4, v28, v28
	v_cndmask_b32_e64 v5, v27, v26, s[0:1]
	v_and_b32_e32 v9, 0xffff0000, v7
	v_max_f32_e32 v4, 0xc6ea6000, v4
	v_sub_f32_e32 v9, v7, v9
	v_lshrrev_b32_e32 v7, 16, v7
	v_cndmask_b32_e64 v4, v4, 1.0, s[0:1]
	v_and_b32_e32 v6, 0xffff0000, v5
	v_and_or_b32 v25, v9, s2, v7
	v_sub_f32_e32 v7, v5, v6
	v_or_b32_sdwa v18, v5, v6 dst_sel:DWORD dst_unused:UNUSED_PAD src0_sel:WORD_1 src1_sel:DWORD
	v_and_b32_e32 v5, 0xffff0000, v4
	v_sub_f32_e32 v6, v4, v5
	v_and_b32_e32 v8, 0xffff0000, v6
	v_sub_f32_e32 v8, v6, v8
	v_lshrrev_b32_e32 v6, 16, v6
	v_or_b32_sdwa v20, v4, v5 dst_sel:DWORD dst_unused:UNUSED_PAD src0_sel:WORD_1 src1_sel:DWORD
	v_or_b32_sdwa v19, v7, v5 dst_sel:DWORD dst_unused:UNUSED_PAD src0_sel:WORD_1 src1_sel:DWORD
	v_and_or_b32 v21, v8, s2, v6
	s_mov_b64 s[2:3], 0
	s_cbranch_scc1 .LBB3_11
	s_cmp_gt_i32 s26, 4
	s_cbranch_scc0 .LBB3_14
	s_cmp_gt_i32 s26, 5
	s_cbranch_scc0 .LBB3_15
	s_cmp_eq_u32 s26, 6
	s_mov_b64 s[4:5], 0
	s_cbranch_scc0 .LBB3_48
	v_and_b32_e32 v4, 0xffff0000, v2
	v_max_f32_e32 v3, v3, v3
	v_sub_f32_e32 v4, v2, v4
	v_max_f32_e32 v3, 0xc6ea6000, v3
	v_and_b32_e32 v5, 0xffff0000, v3
	v_and_b32_e32 v4, 0xffff0000, v4
	v_or_b32_sdwa v75, v5, v2 dst_sel:DWORD dst_unused:UNUSED_PAD src0_sel:DWORD src1_sel:WORD_1
	v_or_b32_sdwa v74, v4, v2 dst_sel:DWORD dst_unused:UNUSED_PAD src0_sel:DWORD src1_sel:WORD_1
	v_sub_f32_e32 v2, v3, v5
	v_and_b32_e32 v4, 0xffff0000, v2
	s_mov_b32 s6, 0xffff0000
	v_sub_f32_e32 v4, v2, v4
	v_lshrrev_b32_e32 v2, 16, v2
	v_and_or_b32 v76, v4, s6, v2
	v_or_b32_sdwa v77, v3, v5 dst_sel:DWORD dst_unused:UNUSED_PAD src0_sel:WORD_1 src1_sel:DWORD
	s_movk_i32 s6, 0xfc00
	s_mov_b64 s[8:9], -1
	v_mfma_f32_32x32x16_bf16 v[2:17], v[22:25], v[74:77], 0
	s_nop 11
	v_cvt_pk_f16_f32 v2, v2, v3
	v_cvt_pk_f16_f32 v3, v4, v5
	v_pk_max_i16 v2, v2, s6 op_sel_hi:[1,0]
	v_pk_max_i16 v3, v3, s6 op_sel_hi:[1,0]
	s_nop 0
	v_exp_f16_e32 v43, v2
	v_exp_f16_e32 v45, v3
	v_exp_f16_sdwa v43, v2 dst_sel:WORD_1 dst_unused:UNUSED_PRESERVE src0_sel:WORD_1
	v_exp_f16_sdwa v45, v3 dst_sel:WORD_1 dst_unused:UNUSED_PRESERVE src0_sel:WORD_1
	v_cvt_pk_f16_f32 v2, v6, v7
	v_cvt_pk_f16_f32 v3, v8, v9
	v_pk_max_i16 v2, v2, s6 op_sel_hi:[1,0]
	v_pk_max_i16 v3, v3, s6 op_sel_hi:[1,0]
	s_nop 0
	v_exp_f16_e32 v50, v2
	v_exp_f16_e32 v54, v3
	v_exp_f16_sdwa v50, v2 dst_sel:WORD_1 dst_unused:UNUSED_PRESERVE src0_sel:WORD_1
	v_exp_f16_sdwa v54, v3 dst_sel:WORD_1 dst_unused:UNUSED_PRESERVE src0_sel:WORD_1
	v_cvt_pk_f16_f32 v2, v10, v11
	v_cvt_pk_f16_f32 v3, v12, v13
	v_pk_max_i16 v2, v2, s6 op_sel_hi:[1,0]
	v_pk_max_i16 v3, v3, s6 op_sel_hi:[1,0]
	s_nop 0
	v_exp_f16_e32 v58, v2
	v_exp_f16_e32 v61, v3
	v_exp_f16_sdwa v58, v2 dst_sel:WORD_1 dst_unused:UNUSED_PRESERVE src0_sel:WORD_1
	v_exp_f16_sdwa v61, v3 dst_sel:WORD_1 dst_unused:UNUSED_PRESERVE src0_sel:WORD_1
	v_cvt_pk_f16_f32 v2, v14, v15
	v_cvt_pk_f16_f32 v3, v16, v17
	v_pk_max_i16 v2, v2, s6 op_sel_hi:[1,0]
	v_pk_max_i16 v3, v3, s6 op_sel_hi:[1,0]
	s_nop 0
	v_exp_f16_e32 v64, v2
	v_exp_f16_e32 v66, v3
	v_exp_f16_sdwa v64, v2 dst_sel:WORD_1 dst_unused:UNUSED_PRESERVE src0_sel:WORD_1
	v_exp_f16_sdwa v66, v3 dst_sel:WORD_1 dst_unused:UNUSED_PRESERVE src0_sel:WORD_1
	v_mfma_f32_32x32x16_bf16 v[2:17], v[18:21], v[74:77], 0
	s_nop 11
	v_cvt_pk_f16_f32 v2, v2, v3
	v_cvt_pk_f16_f32 v3, v4, v5
	v_pk_max_i16 v2, v2, s6 op_sel_hi:[1,0]
	v_pk_max_i16 v3, v3, s6 op_sel_hi:[1,0]
	s_nop 0
	v_exp_f16_e32 v72, v2
	v_exp_f16_e32 v76, v3
	v_exp_f16_sdwa v72, v2 dst_sel:WORD_1 dst_unused:UNUSED_PRESERVE src0_sel:WORD_1
	v_exp_f16_sdwa v76, v3 dst_sel:WORD_1 dst_unused:UNUSED_PRESERVE src0_sel:WORD_1
	v_cvt_pk_f16_f32 v2, v6, v7
	v_cvt_pk_f16_f32 v3, v8, v9
	v_pk_max_i16 v2, v2, s6 op_sel_hi:[1,0]
	v_pk_max_i16 v3, v3, s6 op_sel_hi:[1,0]
	s_nop 0
	v_exp_f16_e32 v83, v2
	v_exp_f16_e32 v85, v3
	v_exp_f16_sdwa v83, v2 dst_sel:WORD_1 dst_unused:UNUSED_PRESERVE src0_sel:WORD_1
	v_exp_f16_sdwa v85, v3 dst_sel:WORD_1 dst_unused:UNUSED_PRESERVE src0_sel:WORD_1
	v_cvt_pk_f16_f32 v2, v10, v11
	v_cvt_pk_f16_f32 v3, v12, v13
	v_pk_max_i16 v2, v2, s6 op_sel_hi:[1,0]
	v_pk_max_i16 v3, v3, s6 op_sel_hi:[1,0]
	s_nop 0
	v_exp_f16_e32 v89, v2
	v_exp_f16_e32 v92, v3
	v_exp_f16_sdwa v89, v2 dst_sel:WORD_1 dst_unused:UNUSED_PRESERVE src0_sel:WORD_1
	v_exp_f16_sdwa v92, v3 dst_sel:WORD_1 dst_unused:UNUSED_PRESERVE src0_sel:WORD_1
	v_cvt_pk_f16_f32 v2, v14, v15
	v_cvt_pk_f16_f32 v3, v16, v17
	v_pk_max_i16 v2, v2, s6 op_sel_hi:[1,0]
	v_pk_max_i16 v3, v3, s6 op_sel_hi:[1,0]
	s_nop 0
	v_exp_f16_e32 v95, v2
	v_exp_f16_e32 v96, v3
	v_exp_f16_sdwa v95, v2 dst_sel:WORD_1 dst_unused:UNUSED_PRESERVE src0_sel:WORD_1
	v_exp_f16_sdwa v96, v3 dst_sel:WORD_1 dst_unused:UNUSED_PRESERVE src0_sel:WORD_1
	s_and_b64 vcc, exec, s[4:5]
	s_cbranch_vccnz .LBB3_16
	s_branch .LBB3_17

_Z6k_iterILb0ELb1EEvPKfS1_PKiPK15HIP_vector_typeIfLj4EES7_S1_S1_S3_S1_PfS8_S1_S3_PDF16_PS5_SA_PiSA_SB_:
	s_and_b32 s38, s0, 0xfffff000
	s_mov_b32 s39, s1
	s_load_dwordx2 s[8:9], s[0:1], 0x80
	s_load_dwordx4 s[4:7], s[0:1], 0x70
	s_load_dwordx4 s[16:19], s[0:1], 0x40
	s_load_dwordx2 s[40:41], s[0:1], 0x90
	s_load_dwordx2 s[22:23], s[0:1], 0x50
	s_load_dwordx2 s[42:43], s[0:1], 0x88
	v_readfirstlane_b32 s12, v0
	v_cmp_gt_u32_e64 s[14:15], 64, v0
	v_lshlrev_b32_e32 v1, 2, v0
	s_and_saveexec_b64 s[10:11], s[14:15]
	v_mov_b32_e32 v2, 0
	ds_write_b32 v1, v2 offset:5152
	s_or_b64 exec, exec, s[10:11]
	s_lshl_b32 s3, s2, 5
	s_and_b32 s3, s3, 0xe0
	s_lshr_b32 s2, s2, 3
	s_add_i32 s2, s3, s2
	s_lshl_b32 s29, s2, 6
	v_and_b32_e32 v2, 31, v0
	v_or_b32_e32 v4, s29, v2
	v_mov_b32_e32 v5, 0
	s_lshr_b32 s30, s12, 6
	s_lshl_b32 s32, s30, 2
	s_lshr_b32 s32, 0x73261540, s32
	s_lshl_b32 s32, s32, 5
	s_and_b32 s32, s32, 0xe0
	v_or_b32_e32 v176, s32, v2
	v_lshlrev_b32_e32 v177, 4, v176
	v_add_u32_e32 v178, 0x1000, v177
	v_add_u32_e32 v179, 0x2000, v177
	v_add_u32_e32 v180, 0x3000, v177
	v_add_u32_e32 v181, 0x4000, v177
	v_add_u32_e32 v182, 0x5000, v177
	s_mov_b32 s3, 0
	s_lshl_b64 s[34:35], s[2:3], 16
	s_lshl_b32 s33, s2, 2
	s_waitcnt lgkmcnt(0)
	s_load_dword s26, s[8:9], s33 offset:0x0
	s_load_dword s41, s[40:41], s33 offset:0x0
	s_add_u32 s20, s4, s34
	s_addc_u32 s21, s5, s35
	v_lshl_add_u64 v[4:5], v[4:5], 4, s[6:7]
	global_load_dwordx3 v[30:32], v[4:5], off
	global_load_dwordx3 v[26:28], v[4:5], off offset:512
	global_load_dwordx4 v[2:5], v177, s[20:21]
	global_load_dwordx4 v[6:9], v178, s[20:21]
	global_load_dwordx4 v[10:13], v179, s[20:21]
	global_load_dwordx4 v[14:17], v180, s[20:21]
	global_load_dwordx4 v[18:21], v181, s[20:21]
	global_load_dwordx4 v[22:25], v182, s[20:21]
	s_lshl_b32 s46, s30, 12
	s_add_u32 s46, s46, 0x8000
	s_add_u32 s44, s20, s46
	s_addc_u32 s45, s21, 0
	s_add_u32 s36, s42, s34
	s_addc_u32 s37, s43, s35
	s_add_u32 s36, s36, s46
	s_addc_u32 s37, s37, 0
	v_and_b32_e32 v183, 63, v0
	v_lshlrev_b32_e32 v183, 4, v183
	global_load_dwordx4 v[184:187], v183, s[44:45]
	global_load_dwordx4 v[188:191], v183, s[44:45] offset:1024
	global_load_dwordx4 v[192:195], v183, s[44:45] offset:2048
	global_load_dwordx4 v[196:199], v183, s[44:45] offset:3072
	global_load_dwordx4 v[200:203], v183, s[36:37]
	global_load_dwordx4 v[204:207], v183, s[36:37] offset:1024
	global_load_dwordx4 v[208:211], v183, s[36:37] offset:2048
	global_load_dwordx4 v[212:215], v183, s[36:37] offset:3072
	v_and_b32_e32 v38, 63, v0
	v_mov_b32_e32 v29, 0xff800000
	v_cmp_gt_u32_e64 s[0:1], 32, v38
	s_waitcnt lgkmcnt(0)
	s_cmpk_gt_i32 s26, 0x600
	s_cselect_b64 s[24:25], -1, 0
	s_cmpk_lt_i32 s26, 0x601
	s_cbranch_scc1 .LBB4_6
	s_and_saveexec_b64 s[8:9], s[14:15]
	s_cbranch_execz .LBB4_5
	v_or_b32_e32 v178, s29, v0
	v_mov_b32_e32 v179, 0
	v_lshl_add_u64 v[178:179], v[178:179], 4, s[6:7]
	global_load_dwordx4 v[178:181], v[178:179], off
	v_lshlrev_b32_e32 v177, 4, v0
	s_waitcnt vmcnt(0)
	ds_write_b128 v177, v[178:181] offset:2080

.LBB4_6:
	s_xor_b32 s33, s32, 0xff
	s_add_i32 s33, s33, s26
	s_ashr_i32 s27, s33, 8
	v_cmp_gt_i32_e32 vcc, s26, v176
	v_med3_i32 v33, s27, 0, 6
	s_sub_i32 s33, s26, 0x100
	v_cmp_gt_i32_e64 s[4:5], s33, v176
	s_sub_i32 s33, s26, 0x200
	v_cmp_gt_i32_e64 s[6:7], s33, v176
	s_sub_i32 s33, s26, 0x300
	v_cmp_gt_i32_e64 s[8:9], s33, v176
	s_sub_i32 s33, s26, 0x400
	v_cmp_gt_i32_e64 s[10:11], s33, v176
	s_sub_i32 s33, s26, 0x500
	v_cmp_gt_i32_e64 s[12:13], s33, v176
	s_and_b32 s27, s29, 0x7ffff000
	s_mov_b32 s2, 0xffff0000
	v_readfirstlane_b32 s28, v33
	s_nop 3
	s_cmp_lt_i32 s28, 4
	s_waitcnt vmcnt(13)
	v_cndmask_b32_e32 v4, v29, v4, vcc
	v_cndmask_b32_e64 v134, v3, v2, s[0:1]
	v_cndmask_b32_e32 v134, 0, v134, vcc
	s_waitcnt vmcnt(12)
	v_cndmask_b32_e64 v3, v29, v8, s[4:5]
	v_cndmask_b32_e64 v97, v7, v6, s[0:1]
	v_cndmask_b32_e64 v97, 0, v97, s[4:5]
	v_cndmask_b32_e64 v135, 1.0, v4, s[0:1]
	v_cndmask_b32_e64 v33, -1, v9, s[4:5]
	v_cndmask_b32_e64 v98, 1.0, v3, s[0:1]
	s_waitcnt vmcnt(11)
	v_cndmask_b32_e64 v6, v29, v12, s[6:7]
	v_cndmask_b32_e64 v68, v11, v10, s[0:1]
	v_cndmask_b32_e64 v68, 0, v68, s[6:7]
	s_waitcnt vmcnt(10)
	v_cndmask_b32_e64 v7, v29, v16, s[8:9]
	v_cndmask_b32_e64 v70, 1.0, v6, s[0:1]
	v_cndmask_b32_e64 v73, 1.0, v7, s[0:1]
	v_cndmask_b32_e64 v34, -1, v13, s[6:7]
	v_cndmask_b32_e64 v35, -1, v17, s[8:9]
	v_cndmask_b32_e64 v71, v15, v14, s[0:1]
	v_cndmask_b32_e64 v71, 0, v71, s[8:9]
	s_waitcnt vmcnt(9)
	v_cndmask_b32_e64 v8, v29, v20, s[10:11]
	v_cndmask_b32_e64 v48, 1.0, v8, s[0:1]
	s_waitcnt vmcnt(8)
	v_cndmask_b32_e64 v10, v29, v24, s[12:13]
	v_cndmask_b32_e32 v29, -1, v5, vcc
	v_max_i32_e32 v4, 0, v29
	v_add_u32_e32 v4, s27, v4
	v_mov_b32_e32 v5, 0
	v_lshl_add_u64 v[6:7], v[4:5], 2, s[16:17]
	v_max_i32_e32 v4, 0, v33
	v_add_u32_e32 v4, s27, v4
	v_lshl_add_u64 v[8:9], v[4:5], 2, s[16:17]
	v_max_i32_e32 v4, 0, v34
	v_add_u32_e32 v4, s27, v4
	v_cndmask_b32_e64 v3, 1.0, v10, s[0:1]
	v_lshl_add_u64 v[10:11], v[4:5], 2, s[16:17]
	v_max_i32_e32 v4, 0, v35
	v_cndmask_b32_e64 v36, -1, v21, s[10:11]
	v_add_u32_e32 v4, s27, v4
	v_lshl_add_u64 v[12:13], v[4:5], 2, s[16:17]
	v_max_i32_e32 v4, 0, v36
	v_cndmask_b32_e64 v37, -1, v25, s[12:13]
	v_add_u32_e32 v4, s27, v4
	v_lshl_add_u64 v[14:15], v[4:5], 2, s[16:17]
	v_max_i32_e32 v4, 0, v37
	v_cndmask_b32_e64 v46, v19, v18, s[0:1]
	v_cndmask_b32_e64 v46, 0, v46, s[10:11]
	v_cndmask_b32_e64 v2, v23, v22, s[0:1]
	v_cndmask_b32_e64 v2, 0, v2, s[12:13]
	v_add_u32_e32 v4, s27, v4
	v_lshl_add_u64 v[4:5], v[4:5], 2, s[16:17]
	s_cmpk_lt_i32 s26, 0x801
	s_cselect_b32 s47, 1, 0
	s_cbranch_scc0 .Lftc_nocache
	s_lshl_b32 s46, s30, 12
	s_add_u32 s46, s46, 0x8000
	s_add_u32 s44, s20, s46
	s_addc_u32 s45, s21, 0
	v_lshlrev_b32_e32 v183, 4, v38
.Lftc_nocache:
	s_cmpk_lt_i32 s41, 0x801
	s_cselect_b32 s36, 1, 0
	s_cbranch_scc0 .Lftc_nocache1
	s_lshl_b32 s46, s30, 12
	s_add_u32 s46, s46, 0x8000
	s_add_u32 s44, s42, s34
	s_addc_u32 s45, s43, s35
	s_add_u32 s44, s44, s46
	s_addc_u32 s45, s45, 0
	v_lshlrev_b32_e32 v183, 4, v38
.Lftc_nocache1:
	s_cmp_lt_i32 s28, 4
	global_load_dword v133, v[6:7], off
	global_load_dword v132, v[8:9], off
	global_load_dword v131, v[10:11], off
	global_load_dword v130, v[12:13], off
	global_load_dword v129, v[14:15], off
	global_load_dword v128, v[4:5], off
	v_max_f32_e32 v6, v32, v32
	v_cndmask_b32_e64 v4, v31, v30, s[0:1]
	v_max_f32_e32 v6, 0xc6ea6000, v6
	v_cndmask_b32_e64 v6, v6, 1.0, s[0:1]
	v_and_b32_e32 v7, 0xffff0000, v4
	v_sub_f32_e32 v8, v4, v7
	v_or_b32_sdwa v22, v4, v7 dst_sel:DWORD dst_unused:UNUSED_PAD src0_sel:WORD_1 src1_sel:DWORD
	v_and_b32_e32 v4, 0xffff0000, v6
	v_sub_f32_e32 v7, v6, v4
	v_or_b32_sdwa v24, v6, v4 dst_sel:DWORD dst_unused:UNUSED_PAD src0_sel:WORD_1 src1_sel:DWORD
	v_or_b32_sdwa v23, v8, v4 dst_sel:DWORD dst_unused:UNUSED_PAD src0_sel:WORD_1 src1_sel:DWORD
	v_max_f32_e32 v4, v28, v28
	v_cndmask_b32_e64 v5, v27, v26, s[0:1]
	v_and_b32_e32 v9, 0xffff0000, v7
	v_max_f32_e32 v4, 0xc6ea6000, v4
	v_sub_f32_e32 v9, v7, v9
	v_lshrrev_b32_e32 v7, 16, v7
	v_cndmask_b32_e64 v4, v4, 1.0, s[0:1]
	v_and_b32_e32 v6, 0xffff0000, v5
	v_and_or_b32 v25, v9, s2, v7
	v_sub_f32_e32 v7, v5, v6
	v_or_b32_sdwa v18, v5, v6 dst_sel:DWORD dst_unused:UNUSED_PAD src0_sel:WORD_1 src1_sel:DWORD
	v_and_b32_e32 v5, 0xffff0000, v4
	v_sub_f32_e32 v6, v4, v5
	v_and_b32_e32 v8, 0xffff0000, v6
	v_sub_f32_e32 v8, v6, v8
	v_lshrrev_b32_e32 v6, 16, v6
	v_or_b32_sdwa v20, v4, v5 dst_sel:DWORD dst_unused:UNUSED_PAD src0_sel:WORD_1 src1_sel:DWORD
	v_or_b32_sdwa v19, v7, v5 dst_sel:DWORD dst_unused:UNUSED_PAD src0_sel:WORD_1 src1_sel:DWORD
	v_and_or_b32 v21, v8, s2, v6
	s_mov_b64 s[2:3], 0
	s_cbranch_scc1 .LBB4_11
	s_cmp_gt_i32 s28, 4
	s_cbranch_scc0 .LBB4_14
	s_cmp_gt_i32 s28, 5
	s_cbranch_scc0 .LBB4_15
	s_cmp_eq_u32 s28, 6
	s_mov_b64 s[4:5], 0
	s_cbranch_scc0 .LBB4_48
	v_and_b32_e32 v4, 0xffff0000, v2
	v_max_f32_e32 v3, v3, v3
	v_sub_f32_e32 v4, v2, v4
	v_max_f32_e32 v3, 0xc6ea6000, v3
	v_and_b32_e32 v5, 0xffff0000, v3
	v_and_b32_e32 v4, 0xffff0000, v4
	v_or_b32_sdwa v75, v5, v2 dst_sel:DWORD dst_unused:UNUSED_PAD src0_sel:DWORD src1_sel:WORD_1
	v_or_b32_sdwa v74, v4, v2 dst_sel:DWORD dst_unused:UNUSED_PAD src0_sel:DWORD src1_sel:WORD_1
	v_sub_f32_e32 v2, v3, v5
	v_and_b32_e32 v4, 0xffff0000, v2
	s_mov_b32 s6, 0xffff0000
	v_sub_f32_e32 v4, v2, v4
	v_lshrrev_b32_e32 v2, 16, v2
	v_and_or_b32 v76, v4, s6, v2
	v_or_b32_sdwa v77, v3, v5 dst_sel:DWORD dst_unused:UNUSED_PAD src0_sel:WORD_1 src1_sel:DWORD
	s_movk_i32 s6, 0xfc00
	s_mov_b64 s[8:9], -1
	v_mfma_f32_32x32x16_bf16 v[2:17], v[22:25], v[74:77], 0
	s_nop 11
	v_cvt_pk_f16_f32 v2, v2, v3
	v_cvt_pk_f16_f32 v3, v4, v5
	v_pk_max_i16 v2, v2, s6 op_sel_hi:[1,0]
	v_pk_max_i16 v3, v3, s6 op_sel_hi:[1,0]
	s_nop 0
	v_exp_f16_e32 v43, v2
	v_exp_f16_e32 v45, v3
	v_exp_f16_sdwa v43, v2 dst_sel:WORD_1 dst_unused:UNUSED_PRESERVE src0_sel:WORD_1
	v_exp_f16_sdwa v45, v3 dst_sel:WORD_1 dst_unused:UNUSED_PRESERVE src0_sel:WORD_1
	v_cvt_pk_f16_f32 v2, v6, v7
	v_cvt_pk_f16_f32 v3, v8, v9
	v_pk_max_i16 v2, v2, s6 op_sel_hi:[1,0]
	v_pk_max_i16 v3, v3, s6 op_sel_hi:[1,0]
	s_nop 0
	v_exp_f16_e32 v50, v2
	v_exp_f16_e32 v54, v3
	v_exp_f16_sdwa v50, v2 dst_sel:WORD_1 dst_unused:UNUSED_PRESERVE src0_sel:WORD_1
	v_exp_f16_sdwa v54, v3 dst_sel:WORD_1 dst_unused:UNUSED_PRESERVE src0_sel:WORD_1
	v_cvt_pk_f16_f32 v2, v10, v11
	v_cvt_pk_f16_f32 v3, v12, v13
	v_pk_max_i16 v2, v2, s6 op_sel_hi:[1,0]
	v_pk_max_i16 v3, v3, s6 op_sel_hi:[1,0]
	s_nop 0
	v_exp_f16_e32 v58, v2
	v_exp_f16_e32 v61, v3
	v_exp_f16_sdwa v58, v2 dst_sel:WORD_1 dst_unused:UNUSED_PRESERVE src0_sel:WORD_1
	v_exp_f16_sdwa v61, v3 dst_sel:WORD_1 dst_unused:UNUSED_PRESERVE src0_sel:WORD_1
	v_cvt_pk_f16_f32 v2, v14, v15
	v_cvt_pk_f16_f32 v3, v16, v17
	v_pk_max_i16 v2, v2, s6 op_sel_hi:[1,0]
	v_pk_max_i16 v3, v3, s6 op_sel_hi:[1,0]
	s_nop 0
	v_exp_f16_e32 v64, v2
	v_exp_f16_e32 v66, v3
	v_exp_f16_sdwa v64, v2 dst_sel:WORD_1 dst_unused:UNUSED_PRESERVE src0_sel:WORD_1
	v_exp_f16_sdwa v66, v3 dst_sel:WORD_1 dst_unused:UNUSED_PRESERVE src0_sel:WORD_1
	v_mfma_f32_32x32x16_bf16 v[2:17], v[18:21], v[74:77], 0
	s_nop 11
	v_cvt_pk_f16_f32 v2, v2, v3
	v_cvt_pk_f16_f32 v3, v4, v5
	v_pk_max_i16 v2, v2, s6 op_sel_hi:[1,0]
	v_pk_max_i16 v3, v3, s6 op_sel_hi:[1,0]
	s_nop 0
	v_exp_f16_e32 v72, v2
	v_exp_f16_e32 v76, v3
	v_exp_f16_sdwa v72, v2 dst_sel:WORD_1 dst_unused:UNUSED_PRESERVE src0_sel:WORD_1
	v_exp_f16_sdwa v76, v3 dst_sel:WORD_1 dst_unused:UNUSED_PRESERVE src0_sel:WORD_1
	v_cvt_pk_f16_f32 v2, v6, v7
	v_cvt_pk_f16_f32 v3, v8, v9
	v_pk_max_i16 v2, v2, s6 op_sel_hi:[1,0]
	v_pk_max_i16 v3, v3, s6 op_sel_hi:[1,0]
	s_nop 0
	v_exp_f16_e32 v83, v2
	v_exp_f16_e32 v85, v3
	v_exp_f16_sdwa v83, v2 dst_sel:WORD_1 dst_unused:UNUSED_PRESERVE src0_sel:WORD_1
	v_exp_f16_sdwa v85, v3 dst_sel:WORD_1 dst_unused:UNUSED_PRESERVE src0_sel:WORD_1
	v_cvt_pk_f16_f32 v2, v10, v11
	v_cvt_pk_f16_f32 v3, v12, v13
	v_pk_max_i16 v2, v2, s6 op_sel_hi:[1,0]
	v_pk_max_i16 v3, v3, s6 op_sel_hi:[1,0]
	s_nop 0
	v_exp_f16_e32 v89, v2
	v_exp_f16_e32 v92, v3
	v_exp_f16_sdwa v89, v2 dst_sel:WORD_1 dst_unused:UNUSED_PRESERVE src0_sel:WORD_1
	v_exp_f16_sdwa v92, v3 dst_sel:WORD_1 dst_unused:UNUSED_PRESERVE src0_sel:WORD_1
	v_cvt_pk_f16_f32 v2, v14, v15
	v_cvt_pk_f16_f32 v3, v16, v17
	v_pk_max_i16 v2, v2, s6 op_sel_hi:[1,0]
	v_pk_max_i16 v3, v3, s6 op_sel_hi:[1,0]
	s_nop 0
	v_exp_f16_e32 v95, v2
	v_exp_f16_e32 v96, v3
	v_exp_f16_sdwa v95, v2 dst_sel:WORD_1 dst_unused:UNUSED_PRESERVE src0_sel:WORD_1
	v_exp_f16_sdwa v96, v3 dst_sel:WORD_1 dst_unused:UNUSED_PRESERVE src0_sel:WORD_1
	s_and_b64 vcc, exec, s[4:5]
	s_cbranch_vccnz .LBB4_16
	s_branch .LBB4_17

.LBB4_39:
	s_waitcnt vmcnt(5)
	v_rcp_f32_e32 v2, v133
	s_waitcnt vmcnt(4)
	v_rcp_f32_e32 v3, v132
	s_waitcnt vmcnt(3)
	v_rcp_f32_e32 v4, v131
	v_cmp_lt_f32_e32 vcc, 0, v133
	s_waitcnt vmcnt(2)
	v_rcp_f32_e32 v5, v130
	s_waitcnt vmcnt(1)
	v_rcp_f32_e32 v6, v129
	v_cndmask_b32_e32 v2, 0, v2, vcc
	v_cmp_lt_f32_e32 vcc, 0, v132
	s_waitcnt vmcnt(0)
	v_rcp_f32_e32 v7, v128
	s_getpc_b64 s[36:37]
	s_sub_u32 s36, s36, 0x97bc
	s_subb_u32 s37, s37, 0
	v_lshlrev_b32_e32 v183, 6, v0
	v_min_u32_e32 v183, 0x1d80, v183
	global_load_dword v183, v183, s[36:37]
	v_lshlrev_b32_e32 v182, 6, v38
	global_load_dword v182, v182, s[38:39]
	s_lshl_b32 s40, s29, 10
	s_add_u32 s40, s42, s40
	s_addc_u32 s41, s43, 0
	v_lshlrev_b32_e32 v181, 6, v0
	v_and_b32_e32 v181, 0x7fc0, v181
	global_load_dword v181, v181, s[40:41]
	s_mov_b32 s4, 0x42c80000
	v_cndmask_b32_e32 v3, 0, v3, vcc
	v_cmp_lt_f32_e32 vcc, 0, v131
	v_cmp_ngt_f32_e64 s[2:3], s4, v3
	s_mov_b64 s[6:7], 0
	v_cndmask_b32_e32 v4, 0, v4, vcc
	v_cmp_lt_f32_e32 vcc, 0, v130
	s_nop 1
	v_cndmask_b32_e32 v5, 0, v5, vcc
	v_cmp_lt_f32_e32 vcc, 0, v129
	s_nop 1
	v_cndmask_b32_e32 v6, 0, v6, vcc
	v_cmp_lt_f32_e32 vcc, 0, v128
	s_nop 1
	v_cndmask_b32_e32 v7, 0, v7, vcc
	v_cmp_ngt_f32_e32 vcc, s4, v2
	s_or_b64 s[2:3], vcc, s[2:3]
	v_cmp_ngt_f32_e32 vcc, s4, v4
	s_or_b64 s[2:3], s[2:3], vcc
	v_cmp_ngt_f32_e32 vcc, s4, v5
	s_or_b64 s[2:3], s[2:3], vcc
	v_cmp_ngt_f32_e32 vcc, s4, v6
	s_or_b64 s[2:3], s[2:3], vcc
	v_cmp_ngt_f32_e32 vcc, s4, v7
	s_or_b64 s[2:3], s[2:3], vcc
	v_cndmask_b32_e64 v8, 0, 1, s[2:3]
	v_cmp_ne_u32_e32 vcc, 0, v8
	s_cmp_eq_u64 vcc, 0
	s_cselect_b64 s[2:3], -1, 0
	v_cndmask_b32_e64 v8, 0, 1, s[2:3]
	s_nop 0
	v_readfirstlane_b32 s2, v8
	s_bitcmp0_b32 s2, 0
	s_cbranch_scc0 .LBB4_45
	s_cmp_lt_i32 s28, 4
	s_cbranch_scc1 .LBB4_46
	s_cmp_gt_i32 s28, 4
	s_cbranch_scc0 .LBB4_47
	s_mov_b64 s[4:5], -1
	v_mov_b32_e32 v8, 0
	s_cmp_gt_i32 s28, 5
	v_mov_b32_e32 v167, 0
	v_mov_b32_e32 v166, 0
	v_mov_b32_e32 v165, 0
	v_mov_b32_e32 v164, 0
	v_mov_b32_e32 v162, 0
	v_mov_b32_e32 v160, 0
	v_mov_b32_e32 v159, 0
	v_mov_b32_e32 v157, 0
	v_mov_b32_e32 v151, 0
	v_mov_b32_e32 v149, 0
	v_mov_b32_e32 v147, 0
	v_mov_b32_e32 v146, 0
	v_mov_b32_e32 v144, 0
	v_mov_b32_e32 v143, 0
	v_mov_b32_e32 v152, 0
	v_mov_b32_e32 v153, 0
	v_mov_b32_e32 v154, 0
	v_mov_b32_e32 v155, 0
	v_mov_b32_e32 v156, 0
	v_mov_b32_e32 v158, 0
	v_mov_b32_e32 v161, 0
	v_mov_b32_e32 v163, 0
	v_mov_b32_e32 v168, 0
	v_mov_b32_e32 v169, 0
	v_mov_b32_e32 v170, 0
	v_mov_b32_e32 v171, 0
	v_mov_b32_e32 v172, 0
	v_mov_b32_e32 v173, 0
	v_mov_b32_e32 v174, 0
	v_mov_b32_e32 v145, 0
	v_mov_b32_e32 v148, 0
	v_mov_b32_e32 v150, 0
	s_cbranch_scc0 .LBB4_50
	s_cmp_eq_u32 s28, 6
	s_cbranch_scc0 .LBB4_49
	v_mov_b32_e32 v145, 0
	v_mov_b32_e32 v148, 0
	v_mov_b32_e32 v150, 0
	v_mov_b32_e32 v143, 0
	v_mov_b32_e32 v144, 0
	v_mov_b32_e32 v146, 0
	v_mov_b32_e32 v147, 0
	v_mov_b32_e32 v149, 0
	v_mov_b32_e32 v151, 0
	v_mov_b32_e32 v152, 0
	v_mov_b32_e32 v153, 0
	v_mov_b32_e32 v154, 0
	v_mov_b32_e32 v155, 0
	v_mov_b32_e32 v156, 0
	v_mov_b32_e32 v158, 0
	v_mov_b32_e32 v161, 0
	v_mov_b32_e32 v163, 0
	v_mov_b32_e32 v157, 0
	v_mov_b32_e32 v159, 0
	v_mov_b32_e32 v160, 0
	v_mov_b32_e32 v162, 0
	v_mov_b32_e32 v164, 0
	v_mov_b32_e32 v165, 0
	v_mov_b32_e32 v166, 0
	v_mov_b32_e32 v167, 0
	v_mov_b32_e32 v168, 0
	v_mov_b32_e32 v169, 0
	v_mov_b32_e32 v170, 0
	v_mov_b32_e32 v171, 0
	v_mov_b32_e32 v172, 0
	v_mov_b32_e32 v173, 0
	v_mov_b32_e32 v174, 0
	v_fma_mix_f32 v148, v43, v7, v148 op_sel_hi:[1,0,0]
	v_fma_mix_f32 v150, v45, v7, v150 op_sel_hi:[1,0,0]
	v_fma_mix_f32 v143, v50, v7, v143 op_sel_hi:[1,0,0]
	v_fma_mix_f32 v144, v54, v7, v144 op_sel_hi:[1,0,0]
	v_fma_mix_f32 v146, v58, v7, v146 op_sel_hi:[1,0,0]
	v_fma_mix_f32 v147, v61, v7, v147 op_sel_hi:[1,0,0]
	v_fma_mix_f32 v149, v64, v7, v149 op_sel_hi:[1,0,0]
	v_fma_mix_f32 v151, v66, v7, v151 op_sel_hi:[1,0,0]
	v_fma_mix_f32 v152, v43, v7, v152 op_sel:[1,0,0] op_sel_hi:[1,0,0]
	v_fma_mix_f32 v153, v45, v7, v153 op_sel:[1,0,0] op_sel_hi:[1,0,0]
	v_fma_mix_f32 v154, v50, v7, v154 op_sel:[1,0,0] op_sel_hi:[1,0,0]
	v_fma_mix_f32 v155, v54, v7, v155 op_sel:[1,0,0] op_sel_hi:[1,0,0]
	v_fma_mix_f32 v156, v58, v7, v156 op_sel:[1,0,0] op_sel_hi:[1,0,0]
	v_fma_mix_f32 v158, v61, v7, v158 op_sel:[1,0,0] op_sel_hi:[1,0,0]
	v_fma_mix_f32 v161, v64, v7, v161 op_sel:[1,0,0] op_sel_hi:[1,0,0]
	v_fma_mix_f32 v163, v66, v7, v163 op_sel:[1,0,0] op_sel_hi:[1,0,0]
	v_fma_mix_f32 v157, v72, v7, v157 op_sel_hi:[1,0,0]
	v_fma_mix_f32 v159, v76, v7, v159 op_sel_hi:[1,0,0]
	v_fma_mix_f32 v160, v83, v7, v160 op_sel_hi:[1,0,0]
	v_fma_mix_f32 v162, v85, v7, v162 op_sel_hi:[1,0,0]
	v_fma_mix_f32 v164, v89, v7, v164 op_sel_hi:[1,0,0]
	v_fma_mix_f32 v165, v92, v7, v165 op_sel_hi:[1,0,0]
	v_fma_mix_f32 v166, v95, v7, v166 op_sel_hi:[1,0,0]
	v_fma_mix_f32 v167, v96, v7, v167 op_sel_hi:[1,0,0]
	v_fma_mix_f32 v168, v72, v7, v168 op_sel:[1,0,0] op_sel_hi:[1,0,0]
	v_fma_mix_f32 v169, v76, v7, v169 op_sel:[1,0,0] op_sel_hi:[1,0,0]
	v_fma_mix_f32 v170, v83, v7, v170 op_sel:[1,0,0] op_sel_hi:[1,0,0]
	v_fma_mix_f32 v171, v85, v7, v171 op_sel:[1,0,0] op_sel_hi:[1,0,0]
	v_fma_mix_f32 v172, v89, v7, v172 op_sel:[1,0,0] op_sel_hi:[1,0,0]
	v_fma_mix_f32 v173, v92, v7, v173 op_sel:[1,0,0] op_sel_hi:[1,0,0]
	v_fma_mix_f32 v174, v95, v7, v174 op_sel:[1,0,0] op_sel_hi:[1,0,0]
	v_fma_mix_f32 v145, v96, v7, v145 op_sel:[1,0,0] op_sel_hi:[1,0,0]
	s_branch .LBB4_50
